# m11 + gate/up epilogue: +1 of (clamp(up)+1) folded into the bias (64 fewer VALU per lane per unit)
# baseline (speedup 1.0000x reference)
; #define PG8_STAGE(bufoff, rs, soff, voff) do { _Pragma("unroll") for (int _i = 0; _i < 2; ++_i) \
;         __builtin_amdgcn_raw_ptr_buffer_load_lds(rs, (LAS void*)(lds + (bufoff) + ldsw + _i * 8192), 16, (voff), (soff) + _i * ((&(voff) == &voffA) ? pieceA : pieceB), 0, 0); } while (0)
; #define PG8_WAIT_V(n) asm volatile("s_waitcnt vmcnt(" #n ")" ::: "memory")
; #define PG8_BAR __builtin_amdgcn_s_barrier()
; template <class Epi, class Sched, bool FP8 = false>
; __device__ __forceinline__ void gemm_phase(LAS unsigned char* lds, const Gemm g, const Sched& S, const Epi& E, const int wave) {
;     ...
;     PG8_STAGE(PG8_SB(0, 0), rsB, cB, voffB); PG8_STAGE(PG8_SA(0, 0), rsA, cA, voffA); PG8_STAGE(PG8_SB(0, 1), rsB, cB + hstepB, voffB); PG8_STAGE(PG8_SA(0, 1), rsA, cA + hstepA, voffA);
;     if (wr == 1) PG8_BAR;
;     PG8_WAIT_V(4); PG8_BAR;
;     PG8_STAGE(PG8_SB(1, 0), rsB, cB + kstep, voffB); PG8_STAGE(PG8_SA(1, 0), rsA, cA + kstep, voffA); PG8_STAGE(PG8_SB(1, 1), rsB, cB + hstepB + kstep, voffB);
;     PG8_WAIT_V(6); PG8_BAR;
;     __device__ __forceinline__ void operator()(const f32x4 (&acc)[2][2][4][2], const Unit& u, int wr, int wc, int fr, int fq) const {
;     ...
;                     const f32x4 v0 = acc[ai][bj][m][0] * W8_INV + c0v, v1 = acc[ai][bj][m][1] * W8_INV + c1v;
;                     float o[4];
; #pragma unroll
;                     for (int j = 0; j < 4; ++j) { const float gt = fminf(j < 2 ? v0[2 * j] : v1[2 * j - 4], SW_LIMIT); const float up = fminf(fmaxf(j < 2 ? v0[2 * j + 1] : v1[2 * j - 3], -SW_LIMIT), SW_LIMIT);
;                         o[j] = (up + 1.0f) * (gt * __builtin_amdgcn_rcpf(1.0f + __builtin_amdgcn_exp2f(gt * (-SW_ALPHA * 1.4426950408889634f)))); }
.LBB0_1261:
	s_add_i32 s47, s34, 0x18000
	s_or_b32 s7, s75, 0x80
	s_mov_b32 s8, s54
	s_mov_b32 s10, s86
	s_mov_b32 s11, s87
	s_mov_b32 m0, s47
	s_add_i32 s48, s34, 0x1a000
	s_waitcnt vmcnt(4)
	s_barrier
	buffer_load_dwordx4 v139, s[8:11], s7 offen lds
	s_or_b32 s7, s75, 0x20080
	s_mov_b32 m0, s48
	s_add_i32 s49, s34, 0x8000
	buffer_load_dwordx4 v139, s[8:11], s7 offen lds
	s_or_b32 s7, s2, 0x80
	s_mov_b32 m0, s49
	s_add_i32 s50, s34, 0xa000
	buffer_load_dwordx4 v138, s[84:87], s7 offen lds
	s_or_b32 s7, s2, 0x20080
	s_mov_b32 m0, s50
	s_add_i32 s51, s34, 0x1c000
	buffer_load_dwordx4 v138, s[84:87], s7 offen lds
	s_or_b32 s7, s75, 0x40080
	s_mov_b32 m0, s51
	s_add_i32 s52, s34, 0x1e000
	buffer_load_dwordx4 v139, s[8:11], s7 offen lds
	s_or_b32 s7, s75, 0x60080
	s_mov_b32 m0, s52
	s_and_b32 s0, s0, 3
	buffer_load_dwordx4 v139, s[8:11], s7 offen lds
	v_and_b32_e32 v1, 48, v0
	v_lshlrev_b32_e32 v2, 6, v0
	s_movk_i32 s8, 0x3c0
	v_lshlrev_b32_e32 v0, 2, v0
	s_lshl_b32 s53, s6, 6
	s_lshl_b32 s7, s6, 13
	v_and_or_b32 v1, v2, s8, v1
	v_and_b32_e32 v0, 32, v0
	s_lshl_b32 s8, s0, 12
	s_mulk_i32 s6, 0x2400
	v_bitop3_b32 v2, v1, s7, v0 bitop3:0xde
	v_bitop3_b32 v0, v1, s8, v0 bitop3:0xde
	s_waitcnt vmcnt(6)
	s_add_i32 s62, s6, 0
	s_lshl_b32 s7, s0, 5
	s_lshl_b32 s8, s0, 4
	s_add_i32 s62, s62, 0x20800
	v_add_u32_e32 v0, 0, v0
	s_add_i32 s58, s34, 0xc000
	s_lshl_b32 s59, s0, 6
	s_add_i32 s60, s34, 0xe000
	s_sub_i32 s61, s89, s98
	s_add_i32 s63, s62, s8
	v_add_u32_e32 v140, 0x10000, v0
	v_add_u32_e32 v141, 0, v2
	v_mov_b32_e32 v142, 0x7f7f7f7f
	v_add_u32_e32 v143, 0x14000, v0
	v_add_u32_e32 v144, 0x18000, v0
	v_add_u32_e32 v145, 0x1c000, v0
	s_lshl_b32 s64, s7, 2
	v_mov_b32_e32 v137, 0
	s_mov_b32 s0, 0x3c800000
	s_mov_b32 s65, 0xc0c00000
	v_mov_b32_e32 v146, 0x41000000
	s_barrier

; #define PG8_STAGE(bufoff, rs, soff, voff) do { _Pragma("unroll") for (int _i = 0; _i < 2; ++_i) \
;         __builtin_amdgcn_raw_ptr_buffer_load_lds(rs, (LAS void*)(lds + (bufoff) + ldsw + _i * 8192), 16, (voff), (soff) + _i * ((&(voff) == &voffA) ? pieceA : pieceB), 0, 0); } while (0)
; #define PG8_LDA(dst, b, h) do { _Pragma("unroll") for (int m = 0; m < 4; ++m) _Pragma("unroll") for (int k = 0; k < 2; ++k) dst[m][k] = *(const LAS bf16x8*)(lds + PG8_SA(b, h) + aoff + m * 2048 + k * 1024); } while (0)
; #define PG8_LDB(dst, b, h) do { _Pragma("unroll") for (int n = 0; n < 2; ++n) _Pragma("unroll") for (int k = 0; k < 2; ++k) dst[n][k] = *(const LAS bf16x8*)(lds + PG8_SB(b, h) + boff + n * 2048 + k * 1024); } while (0)
; #define PG8_WAIT_V(n) asm volatile("s_waitcnt vmcnt(" #n ")" ::: "memory")
; #define PG8_BAR __builtin_amdgcn_s_barrier()
; template <class Epi, class Sched, bool FP8 = false>
; __device__ __forceinline__ void gemm_phase(LAS unsigned char* lds, const Gemm g, const Sched& S, const Epi& E, const int wave) {
;     ...
;         const bool has_next = S.next(ui + 1, nxt);
;         const unsigned nA = has_next ? nxt.aoff : cA, nB = has_next ? nxt.boff : cB;
;         for (int t = 0; t < nt; t += 2) {
;             const bool last = (t == nt - 2);
;             const unsigned a1 = cA + (unsigned)(t + 1) * kstep;
;             const unsigned a2 = last ? nA : cA + (unsigned)(t + 2) * kstep, b2 = last ? nB : cB + (unsigned)(t + 2) * kstep;
;             const unsigned a3 = a2 + kstep, b3 = b2 + kstep;
;             PG8_LDB(B0, 0, 0); PG8_SCHED; PG8_LDA(At, 0, 0); PG8_STAGE(PG8_SA(1, 1), rsA, a1 + hstepA, voffA);
;             PG8_WAIT_L(8); PG8_BAR; PG8_WAIT_L(0); PG8_MMA(0, 0, At, B0); PG8_BAR; PG8_SCHED;
;             PG8_LDB(B1, 0, 1); PG8_STAGE(PG8_SB(0, 0), rsB, b2, voffB);
;             PG8_BAR; PG8_WAIT_L(0); PG8_MMA(0, 1, At, B1); PG8_BAR;
;             PG8_LDA(At, 0, 1); PG8_STAGE(PG8_SA(0, 0), rsA, a2, voffA);
;             PG8_BAR; PG8_WAIT_L(0); PG8_MMA(1, 0, At, B0); PG8_BAR; PG8_SCHED;
;             PG8_STAGE(PG8_SB(0, 1), rsB, b2 + hstepB, voffB);
;             PG8_WAIT_V(6); PG8_BAR; PG8_MMA(1, 1, At, B1); PG8_BAR;
;             PG8_LDB(B0, 1, 0); PG8_SCHED; PG8_LDA(At, 1, 0); PG8_STAGE(PG8_SA(0, 1), rsA, a2 + hstepA, voffA);
;             PG8_WAIT_L(8); PG8_BAR; PG8_WAIT_L(0); PG8_MMA(0, 0, At, B0); PG8_BAR; PG8_SCHED;
.LBB0_1265:
	ds_read_b128 v[128:131], v140
	ds_read_b128 v[132:135], v140 offset:1024
	ds_read_b128 v[148:151], v140 offset:2048
	ds_read_b128 v[152:155], v140 offset:3072
	s_add_i32 s2, s74, 0xfffa0080
	s_cmp_eq_u32 s88, 12
	s_cselect_b32 s90, s39, s2
	s_cselect_b32 s89, s73, s75
	s_add_i32 s2, s90, 0x80
	s_add_i32 s8, s74, 0xfffe0000
	s_mov_b32 m0, s58
	ds_read_b128 v[156:159], v141
	ds_read_b128 v[160:163], v141 offset:1024
	ds_read_b128 v[164:167], v141 offset:2048
	ds_read_b128 v[168:171], v141 offset:3072
	ds_read_b128 v[172:175], v141 offset:4096
	ds_read_b128 v[176:179], v141 offset:5120
	ds_read_b128 v[180:183], v141 offset:6144
	ds_read_b128 v[184:187], v141 offset:7168
	buffer_load_dwordx4 v138, s[84:87], s8 offen lds
	s_mov_b32 m0, s60
	s_nop 0
	buffer_load_dwordx4 v138, s[84:87], s74 offen lds
	s_waitcnt lgkmcnt(8)
	s_barrier
	s_waitcnt lgkmcnt(0)
	s_setprio 1
	s_waitcnt lgkmcnt(6)
	v_mfma_scale_f32_16x16x128_f8f6f4 v[124:127], v[128:135], v[156:163], v[124:127], v142, v142 op_sel_hi:[0,0,0]
	v_mfma_scale_f32_16x16x128_f8f6f4 v[120:123], v[148:155], v[156:163], v[120:123], v142, v142 op_sel_hi:[0,0,0]
	s_waitcnt lgkmcnt(4)
	v_mfma_scale_f32_16x16x128_f8f6f4 v[116:119], v[128:135], v[164:171], v[116:119], v142, v142 op_sel_hi:[0,0,0]
	v_mfma_scale_f32_16x16x128_f8f6f4 v[112:115], v[148:155], v[164:171], v[112:115], v142, v142 op_sel_hi:[0,0,0]
	s_waitcnt lgkmcnt(2)
	v_mfma_scale_f32_16x16x128_f8f6f4 v[188:191], v[128:135], v[172:179], v[108:111], v142, v142 op_sel_hi:[0,0,0]
	v_mfma_scale_f32_16x16x128_f8f6f4 v[192:195], v[148:155], v[172:179], v[104:107], v142, v142 op_sel_hi:[0,0,0]
	s_waitcnt lgkmcnt(0)
	v_mfma_scale_f32_16x16x128_f8f6f4 v[196:199], v[128:135], v[180:187], v[100:103], v142, v142 op_sel_hi:[0,0,0]
	v_mfma_scale_f32_16x16x128_f8f6f4 v[200:203], v[148:155], v[180:187], v[96:99], v142, v142 op_sel_hi:[0,0,0]
	s_setprio 0
	s_barrier
	s_mov_b32 m0, s35
	s_mov_b32 s8, s54
	s_mov_b32 s10, s86
	s_mov_b32 s11, s87
	s_nop 0
	ds_read_b128 v[96:99], v143
	ds_read_b128 v[100:103], v143 offset:1024
	ds_read_b128 v[104:107], v143 offset:2048
	ds_read_b128 v[108:111], v143 offset:3072
	buffer_load_dwordx4 v139, s[8:11], s89 offen lds
	s_add_i32 s91, s89, 0x20000
	s_mov_b32 m0, s40
	s_nop 0
	buffer_load_dwordx4 v139, s[8:11], s91 offen lds
	s_barrier
	s_waitcnt lgkmcnt(0)
	s_setprio 1
	s_waitcnt lgkmcnt(2)
	v_mfma_scale_f32_16x16x128_f8f6f4 v[204:207], v[96:103], v[156:163], v[92:95], v142, v142 op_sel_hi:[0,0,0]
	s_waitcnt lgkmcnt(0)
	v_mfma_scale_f32_16x16x128_f8f6f4 v[156:159], v[104:111], v[156:163], v[88:91], v142, v142 op_sel_hi:[0,0,0]
	v_mfma_scale_f32_16x16x128_f8f6f4 v[160:163], v[96:103], v[164:171], v[84:87], v142, v142 op_sel_hi:[0,0,0]
	v_mfma_scale_f32_16x16x128_f8f6f4 v[164:167], v[104:111], v[164:171], v[80:83], v142, v142 op_sel_hi:[0,0,0]
	v_mfma_scale_f32_16x16x128_f8f6f4 v[168:171], v[96:103], v[172:179], v[76:79], v142, v142 op_sel_hi:[0,0,0]
	v_mfma_scale_f32_16x16x128_f8f6f4 v[172:175], v[104:111], v[172:179], v[72:75], v142, v142 op_sel_hi:[0,0,0]
	v_mfma_scale_f32_16x16x128_f8f6f4 v[176:179], v[96:103], v[180:187], v[68:71], v142, v142 op_sel_hi:[0,0,0]
	v_mfma_scale_f32_16x16x128_f8f6f4 v[180:183], v[104:111], v[180:187], v[64:67], v142, v142 op_sel_hi:[0,0,0]
	s_setprio 0
	s_mov_b32 m0, s34
	s_barrier
	s_nop 3
	ds_read_b128 v[64:67], v141 offset:16384
	ds_read_b128 v[68:71], v141 offset:17408
	ds_read_b128 v[72:75], v141 offset:18432
	ds_read_b128 v[76:79], v141 offset:19456
	ds_read_b128 v[80:83], v141 offset:20480
	ds_read_b128 v[84:87], v141 offset:21504
	ds_read_b128 v[88:91], v141 offset:22528
	ds_read_b128 v[92:95], v141 offset:23552
	buffer_load_dwordx4 v138, s[84:87], s90 offen lds
	s_add_i32 s91, s90, 0x20000
	s_mov_b32 m0, s41
	s_nop 0
	buffer_load_dwordx4 v138, s[84:87], s91 offen lds
	s_barrier
	s_waitcnt lgkmcnt(0)
	s_setprio 1
	s_waitcnt lgkmcnt(6)
	v_mfma_scale_f32_16x16x128_f8f6f4 v[60:63], v[128:135], v[64:71], v[60:63], v142, v142 op_sel_hi:[0,0,0]
	v_mfma_scale_f32_16x16x128_f8f6f4 v[56:59], v[148:155], v[64:71], v[56:59], v142, v142 op_sel_hi:[0,0,0]
	s_waitcnt lgkmcnt(4)
	v_mfma_scale_f32_16x16x128_f8f6f4 v[52:55], v[128:135], v[72:79], v[52:55], v142, v142 op_sel_hi:[0,0,0]
	v_mfma_scale_f32_16x16x128_f8f6f4 v[48:51], v[148:155], v[72:79], v[48:51], v142, v142 op_sel_hi:[0,0,0]
	s_waitcnt lgkmcnt(2)
	v_mfma_scale_f32_16x16x128_f8f6f4 v[184:187], v[128:135], v[80:87], v[44:47], v142, v142 op_sel_hi:[0,0,0]
	v_mfma_scale_f32_16x16x128_f8f6f4 v[208:211], v[148:155], v[80:87], v[40:43], v142, v142 op_sel_hi:[0,0,0]
	s_waitcnt lgkmcnt(0)
	v_mfma_scale_f32_16x16x128_f8f6f4 v[212:215], v[128:135], v[88:95], v[36:39], v142, v142 op_sel_hi:[0,0,0]
	v_mfma_scale_f32_16x16x128_f8f6f4 v[216:219], v[148:155], v[88:95], v[32:35], v142, v142 op_sel_hi:[0,0,0]
	s_setprio 0
	s_barrier
	s_mov_b32 m0, s42
	s_add_i32 s91, s89, 0x40000
	buffer_load_dwordx4 v139, s[8:11], s91 offen lds
	s_add_i32 s91, s89, 0x60000
	s_mov_b32 m0, s43
	s_nop 0
	buffer_load_dwordx4 v139, s[8:11], s91 offen lds
	s_waitcnt vmcnt(6)
	s_barrier
	s_setprio 1
	v_mfma_scale_f32_16x16x128_f8f6f4 v[220:223], v[96:103], v[64:71], v[28:31], v142, v142 op_sel_hi:[0,0,0]
	v_mfma_scale_f32_16x16x128_f8f6f4 v[224:227], v[104:111], v[64:71], v[24:27], v142, v142 op_sel_hi:[0,0,0]
	v_mfma_scale_f32_16x16x128_f8f6f4 v[228:231], v[96:103], v[72:79], v[20:23], v142, v142 op_sel_hi:[0,0,0]
	v_mfma_scale_f32_16x16x128_f8f6f4 v[232:235], v[104:111], v[72:79], v[16:19], v142, v142 op_sel_hi:[0,0,0]
	v_mfma_scale_f32_16x16x128_f8f6f4 v[236:239], v[96:103], v[80:87], v[12:15], v142, v142 op_sel_hi:[0,0,0]
	v_mfma_scale_f32_16x16x128_f8f6f4 v[240:243], v[104:111], v[80:87], v[8:11], v142, v142 op_sel_hi:[0,0,0]
	v_mfma_scale_f32_16x16x128_f8f6f4 v[244:247], v[96:103], v[88:95], v[0:3], v142, v142 op_sel_hi:[0,0,0]
	v_mfma_scale_f32_16x16x128_f8f6f4 v[248:251], v[104:111], v[88:95], v[4:7], v142, v142 op_sel_hi:[0,0,0]
	s_setprio 0
	s_barrier
; #define PG8_STAGE(bufoff, rs, soff, voff) do { _Pragma("unroll") for (int _i = 0; _i < 2; ++_i) \
;         __builtin_amdgcn_raw_ptr_buffer_load_lds(rs, (LAS void*)(lds + (bufoff) + ldsw + _i * 8192), 16, (voff), (soff) + _i * ((&(voff) == &voffA) ? pieceA : pieceB), 0, 0); } while (0)
; #define PG8_LDA(dst, b, h) do { _Pragma("unroll") for (int m = 0; m < 4; ++m) _Pragma("unroll") for (int k = 0; k < 2; ++k) dst[m][k] = *(const LAS bf16x8*)(lds + PG8_SA(b, h) + aoff + m * 2048 + k * 1024); } while (0)
; #define PG8_LDB(dst, b, h) do { _Pragma("unroll") for (int n = 0; n < 2; ++n) _Pragma("unroll") for (int k = 0; k < 2; ++k) dst[n][k] = *(const LAS bf16x8*)(lds + PG8_SB(b, h) + boff + n * 2048 + k * 1024); } while (0)
; #define PG8_WAIT_V(n) asm volatile("s_waitcnt vmcnt(" #n ")" ::: "memory")
; #define PG8_WAIT_L(n) asm volatile("s_waitcnt lgkmcnt(" #n ")" ::: "memory")
; #define PG8_BAR __builtin_amdgcn_s_barrier()
; #define PG8_SCHED __builtin_amdgcn_sched_barrier(0)
; template <class Epi, class Sched, bool FP8 = false>
; __device__ __forceinline__ void gemm_phase(LAS unsigned char* lds, const Gemm g, const Sched& S, const Epi& E, const int wave) {
;     ...
;             PG8_LDB(B0, 1, 0); PG8_SCHED; PG8_LDA(At, 1, 0); PG8_STAGE(PG8_SA(0, 1), rsA, a2 + hstepA, voffA);
;             PG8_WAIT_L(8); PG8_BAR; PG8_WAIT_L(0); PG8_MMA(0, 0, At, B0); PG8_BAR; PG8_SCHED;
;             PG8_LDB(B1, 1, 1); PG8_STAGE(PG8_SB(1, 0), rsB, b3, voffB);
;             PG8_BAR; PG8_WAIT_L(0); PG8_MMA(0, 1, At, B1); PG8_BAR;
;             PG8_LDA(At, 1, 1); PG8_STAGE(PG8_SA(1, 0), rsA, a3, voffA);
;             PG8_BAR; PG8_WAIT_L(0); PG8_MMA(1, 0, At, B0); PG8_BAR; PG8_SCHED;
;             PG8_STAGE(PG8_SB(1, 1), rsB, b3 + hstepB, voffB);
;             PG8_WAIT_V(6); PG8_BAR; PG8_MMA(1, 1, At, B1); PG8_BAR;
	s_nop 3
	ds_read_b128 v[0:3], v144
	ds_read_b128 v[4:7], v144 offset:1024
	ds_read_b128 v[8:11], v144 offset:2048
	ds_read_b128 v[12:15], v144 offset:3072
	s_mov_b32 m0, s44
	s_add_i32 s91, s90, 0x40000
	ds_read_b128 v[16:19], v141 offset:32768
	ds_read_b128 v[20:23], v141 offset:33792
	ds_read_b128 v[24:27], v141 offset:34816
	ds_read_b128 v[28:31], v141 offset:35840
	ds_read_b128 v[32:35], v141 offset:36864
	ds_read_b128 v[36:39], v141 offset:37888
	ds_read_b128 v[40:43], v141 offset:38912
	ds_read_b128 v[44:47], v141 offset:39936
	buffer_load_dwordx4 v138, s[84:87], s91 offen lds
	s_add_i32 s91, s90, 0x60000
	s_mov_b32 m0, s45
	s_nop 0
	buffer_load_dwordx4 v138, s[84:87], s91 offen lds
	s_waitcnt lgkmcnt(8)
	s_barrier
	s_waitcnt lgkmcnt(0)
	s_setprio 1
	s_waitcnt lgkmcnt(6)
	v_mfma_scale_f32_16x16x128_f8f6f4 v[124:127], v[0:7], v[16:23], v[124:127], v142, v142 op_sel_hi:[0,0,0]
	v_mfma_scale_f32_16x16x128_f8f6f4 v[120:123], v[8:15], v[16:23], v[120:123], v142, v142 op_sel_hi:[0,0,0]
	s_waitcnt lgkmcnt(4)
	v_mfma_scale_f32_16x16x128_f8f6f4 v[116:119], v[0:7], v[24:31], v[116:119], v142, v142 op_sel_hi:[0,0,0]
	v_mfma_scale_f32_16x16x128_f8f6f4 v[112:115], v[8:15], v[24:31], v[112:115], v142, v142 op_sel_hi:[0,0,0]
	s_waitcnt lgkmcnt(2)
	v_mfma_scale_f32_16x16x128_f8f6f4 v[108:111], v[0:7], v[32:39], v[188:191], v142, v142 op_sel_hi:[0,0,0]
	v_mfma_scale_f32_16x16x128_f8f6f4 v[104:107], v[8:15], v[32:39], v[192:195], v142, v142 op_sel_hi:[0,0,0]
	s_waitcnt lgkmcnt(0)
	v_mfma_scale_f32_16x16x128_f8f6f4 v[100:103], v[0:7], v[40:47], v[196:199], v142, v142 op_sel_hi:[0,0,0]
	v_mfma_scale_f32_16x16x128_f8f6f4 v[96:99], v[8:15], v[40:47], v[200:203], v142, v142 op_sel_hi:[0,0,0]
	s_setprio 0
	s_barrier
	s_mov_b32 m0, s47
	s_add_i32 s91, s89, 0x80
	ds_read_b128 v[128:131], v145
	ds_read_b128 v[132:135], v145 offset:1024
	ds_read_b128 v[148:151], v145 offset:2048
	ds_read_b128 v[152:155], v145 offset:3072
	buffer_load_dwordx4 v139, s[8:11], s91 offen lds
	s_add_i32 s91, s89, 0x20080
	s_mov_b32 m0, s48
	s_nop 0
	buffer_load_dwordx4 v139, s[8:11], s91 offen lds
	s_barrier
	s_waitcnt lgkmcnt(0)
	s_setprio 1
	s_waitcnt lgkmcnt(2)
	v_mfma_scale_f32_16x16x128_f8f6f4 v[92:95], v[128:135], v[16:23], v[204:207], v142, v142 op_sel_hi:[0,0,0]
	s_waitcnt lgkmcnt(0)
	v_mfma_scale_f32_16x16x128_f8f6f4 v[88:91], v[148:155], v[16:23], v[156:159], v142, v142 op_sel_hi:[0,0,0]
	v_mfma_scale_f32_16x16x128_f8f6f4 v[84:87], v[128:135], v[24:31], v[160:163], v142, v142 op_sel_hi:[0,0,0]
	v_mfma_scale_f32_16x16x128_f8f6f4 v[80:83], v[148:155], v[24:31], v[164:167], v142, v142 op_sel_hi:[0,0,0]
	v_mfma_scale_f32_16x16x128_f8f6f4 v[76:79], v[128:135], v[32:39], v[168:171], v142, v142 op_sel_hi:[0,0,0]
	v_mfma_scale_f32_16x16x128_f8f6f4 v[72:75], v[148:155], v[32:39], v[172:175], v142, v142 op_sel_hi:[0,0,0]
	v_mfma_scale_f32_16x16x128_f8f6f4 v[68:71], v[128:135], v[40:47], v[176:179], v142, v142 op_sel_hi:[0,0,0]
	v_mfma_scale_f32_16x16x128_f8f6f4 v[64:67], v[148:155], v[40:47], v[180:183], v142, v142 op_sel_hi:[0,0,0]
	s_setprio 0
	s_mov_b32 m0, s49
	s_barrier
	ds_read_b128 v[16:19], v141 offset:49152
	ds_read_b128 v[20:23], v141 offset:50176
	ds_read_b128 v[156:159], v141 offset:51200
	ds_read_b128 v[160:163], v141 offset:52224
	ds_read_b128 v[164:167], v141 offset:53248
	ds_read_b128 v[168:171], v141 offset:54272
	ds_read_b128 v[172:175], v141 offset:55296
	ds_read_b128 v[176:179], v141 offset:56320
	buffer_load_dwordx4 v138, s[84:87], s2 offen lds
	s_add_i32 s90, s90, 0x20080
	s_mov_b32 m0, s50
	s_nop 0
	buffer_load_dwordx4 v138, s[84:87], s90 offen lds
	s_barrier
	s_waitcnt lgkmcnt(0)
	s_setprio 1
	s_waitcnt lgkmcnt(6)
	v_mfma_scale_f32_16x16x128_f8f6f4 v[60:63], v[0:7], v[16:23], v[60:63], v142, v142 op_sel_hi:[0,0,0]
	v_mfma_scale_f32_16x16x128_f8f6f4 v[56:59], v[8:15], v[16:23], v[56:59], v142, v142 op_sel_hi:[0,0,0]
	s_waitcnt lgkmcnt(4)
	v_mfma_scale_f32_16x16x128_f8f6f4 v[52:55], v[0:7], v[156:163], v[52:55], v142, v142 op_sel_hi:[0,0,0]
	v_mfma_scale_f32_16x16x128_f8f6f4 v[48:51], v[8:15], v[156:163], v[48:51], v142, v142 op_sel_hi:[0,0,0]
	s_waitcnt lgkmcnt(2)
	v_mfma_scale_f32_16x16x128_f8f6f4 v[44:47], v[0:7], v[164:171], v[184:187], v142, v142 op_sel_hi:[0,0,0]
	v_mfma_scale_f32_16x16x128_f8f6f4 v[40:43], v[8:15], v[164:171], v[208:211], v142, v142 op_sel_hi:[0,0,0]
	s_waitcnt lgkmcnt(0)
	v_mfma_scale_f32_16x16x128_f8f6f4 v[36:39], v[0:7], v[172:179], v[212:215], v142, v142 op_sel_hi:[0,0,0]
	v_mfma_scale_f32_16x16x128_f8f6f4 v[32:35], v[8:15], v[172:179], v[216:219], v142, v142 op_sel_hi:[0,0,0]
	s_setprio 0
	s_barrier
	s_mov_b32 m0, s51
	s_add_i32 s2, s89, 0x40080
	buffer_load_dwordx4 v139, s[8:11], s2 offen lds
	s_add_i32 s89, s89, 0x60080
	s_mov_b32 m0, s52
	s_nop 0
	buffer_load_dwordx4 v139, s[8:11], s89 offen lds
	s_waitcnt vmcnt(6)
	s_barrier
	s_setprio 1
	v_mfma_scale_f32_16x16x128_f8f6f4 v[28:31], v[128:135], v[16:23], v[220:223], v142, v142 op_sel_hi:[0,0,0]
	v_mfma_scale_f32_16x16x128_f8f6f4 v[24:27], v[148:155], v[16:23], v[224:227], v142, v142 op_sel_hi:[0,0,0]
	v_mfma_scale_f32_16x16x128_f8f6f4 v[20:23], v[128:135], v[156:163], v[228:231], v142, v142 op_sel_hi:[0,0,0]
	v_mfma_scale_f32_16x16x128_f8f6f4 v[16:19], v[148:155], v[156:163], v[232:235], v142, v142 op_sel_hi:[0,0,0]
	v_mfma_scale_f32_16x16x128_f8f6f4 v[12:15], v[128:135], v[164:171], v[236:239], v142, v142 op_sel_hi:[0,0,0]
	v_mfma_scale_f32_16x16x128_f8f6f4 v[8:11], v[148:155], v[164:171], v[240:243], v142, v142 op_sel_hi:[0,0,0]
	v_mfma_scale_f32_16x16x128_f8f6f4 v[0:3], v[128:135], v[172:179], v[244:247], v142, v142 op_sel_hi:[0,0,0]
	v_mfma_scale_f32_16x16x128_f8f6f4 v[4:7], v[148:155], v[172:179], v[248:251], v142, v142 op_sel_hi:[0,0,0]
	s_setprio 0
	s_add_i32 s88, s88, 2
	s_addk_i32 s74, 0x100
	s_addk_i32 s75, 0x100
	s_cmp_gt_u32 s88, 13
	s_barrier
; #define LAS __attribute__((address_space(3)))
; __device__ __forceinline__ unsigned pack4_fp8(float a, float b, float c, float d) { int r = 0; r = __builtin_amdgcn_cvt_pk_fp8_f32(a, b, r, false); r = __builtin_amdgcn_cvt_pk_fp8_f32(c, d, r, true); return (unsigned)r; }
;     __device__ __forceinline__ void operator()(const f32x4 (&acc)[2][2][4][2], const Unit& u, int wr, int wc, int fr, int fq) const {
;         const float* bias = b_gu + (size_t)u.e * (2 * DFF) + u.pn * 256 + wc * 32 + 8 * fq;
;         LAS unsigned char* const buf = lds + LDS_EPI + wr * 9216;
; #pragma unroll
;         for (int ai = 0; ai < 2; ++ai) {
; #pragma unroll
;             for (int bj = 0; bj < 2; ++bj) { const f32x4 c0v = ld4(bias + bj * 128), c1v = ld4(bias + bj * 128 + 4);
; #pragma unroll
;                 for (int m = 0; m < 4; ++m) {
;                     const f32x4 v0 = acc[ai][bj][m][0] * W8_INV + c0v, v1 = acc[ai][bj][m][1] * W8_INV + c1v;
;                     float o[4];
; #pragma unroll
;                     for (int j = 0; j < 4; ++j) { const float gt = fminf(j < 2 ? v0[2 * j] : v1[2 * j - 4], SW_LIMIT); const float up = fminf(fmaxf(j < 2 ? v0[2 * j + 1] : v1[2 * j - 3], -SW_LIMIT), SW_LIMIT);
;                         o[j] = (up + 1.0f) * (gt * __builtin_amdgcn_rcpf(1.0f + __builtin_amdgcn_exp2f(gt * (-SW_ALPHA * 1.4426950408889634f)))); }
;                     *(LAS unsigned*)(buf + (m * 16 + fr) * 144 + bj * 64 + wc * 16 + fq * 4) = pack4_fp8(o[0], o[1], o[2], o[3]); } }
	s_cbranch_scc0 .LBB0_1265
	s_ashr_i32 s39, s38, 31
	v_readlane_b32 s16, v254, 22
	s_lshl_b64 s[10:11], s[38:39], 14
	v_readlane_b32 s18, v254, 24
	v_readlane_b32 s19, v254, 25
	s_add_u32 s2, s18, s10
	s_addc_u32 s8, s19, s11
	s_lshl_b32 s10, s71, 8
	s_ashr_i32 s11, s10, 31
	v_mbcnt_lo_u32_b32 v128, -1, 0
	v_mbcnt_hi_u32_b32 v128, -1, v128
	s_lshl_b64 s[10:11], s[10:11], 2
	v_bfe_u32 v129, v128, 4, 2
	v_and_b32_e32 v150, 15, v128
	s_add_u32 s2, s2, s10
	v_lshlrev_b32_e32 v149, 5, v129
	v_lshlrev_b32_e32 v151, 2, v129
	v_lshlrev_b32_e32 v129, 4, v129
	v_lshlrev_b32_e32 v128, 4, v128
	s_addc_u32 s8, s8, s11
	v_and_b32_e32 v136, 0x70, v128
	v_or3_b32 v128, v129, s59, v150
	s_add_u32 s10, s2, s64
	v_lshrrev_b32_e32 v148, 3, v128
	s_addc_u32 s11, s8, 0
	v_mul_u32_u24_e32 v128, 0x90, v148
	v_add3_u32 v147, s62, v136, v128
	global_load_dwordx4 v[128:131], v149, s[10:11] offset:16
	global_load_dwordx4 v[132:135], v149, s[10:11]
	s_lshl_b32 s8, s72, 8
	s_add_i32 s8, s8, s53
	s_lshl_b32 s38, s71, 7
	s_ashr_i32 s39, s38, 31
	s_and_b64 vcc, exec, s[6:7]
	s_mov_b32 s71, s66
	s_mov_b32 s72, s68
	s_mov_b32 s75, s69
	s_mov_b32 s2, s70
	v_readlane_b32 s17, v254, 23
	v_readlane_b32 s20, v254, 26
	v_readlane_b32 s21, v254, 27
	v_readlane_b32 s22, v254, 28
	v_readlane_b32 s23, v254, 29
	v_readlane_b32 s24, v254, 30
	v_readlane_b32 s25, v254, 31
	v_readlane_b32 s26, v254, 32
	v_readlane_b32 s27, v254, 33
	v_readlane_b32 s28, v254, 34
	v_readlane_b32 s29, v254, 35
	v_readlane_b32 s30, v254, 36
	v_readlane_b32 s31, v254, 37
	s_waitcnt vmcnt(0)
	v_add_f32_e32 v129, 1.0, v129
	v_add_f32_e32 v131, 1.0, v131
	v_add_f32_e32 v133, 1.0, v133
	v_add_f32_e32 v135, 1.0, v135
	v_pk_fma_f32 v[120:121], v[120:121], s[0:1], v[128:129] op_sel_hi:[1,0,1]
	s_waitcnt vmcnt(0)
	v_pk_fma_f32 v[124:125], v[124:125], s[0:1], v[132:133] op_sel_hi:[1,0,1]
	v_pk_fma_f32 v[126:127], v[126:127], s[0:1], v[134:135] op_sel_hi:[1,0,1]
	v_min_f32_e32 v124, 0x40e00000, v124
	v_mul_f32_e32 v152, 0xc01d265f, v124
	v_exp_f32_e32 v152, v152
	v_med3_f32 v125, v125, s65, v146
	v_min_f32_e32 v120, 0x40e00000, v120
	v_add_f32_e32 v152, 1.0, v152
	v_rcp_f32_e32 v152, v152
	v_med3_f32 v121, v121, s65, v146
	v_pk_fma_f32 v[122:123], v[122:123], s[0:1], v[130:131] op_sel_hi:[1,0,1]
	v_mul_f32_e32 v124, v124, v152
	v_mul_f32_e32 v124, v125, v124
	v_min_f32_e32 v125, 0x40e00000, v126
	v_med3_f32 v126, v127, s65, v146
	v_mul_f32_e32 v127, 0xc01d265f, v125
	v_exp_f32_e32 v127, v127
	v_pk_fma_f32 v[116:117], v[116:117], s[0:1], v[132:133] op_sel_hi:[1,0,1]
	v_pk_fma_f32 v[118:119], v[118:119], s[0:1], v[134:135] op_sel_hi:[1,0,1]
	v_add_f32_e32 v127, 1.0, v127
	v_rcp_f32_e32 v127, v127
	v_min_f32_e32 v116, 0x40e00000, v116
	v_med3_f32 v117, v117, s65, v146
	v_mul_f32_e32 v125, v125, v127
	v_mul_f32_e32 v125, v126, v125
	v_mul_f32_e32 v126, 0xc01d265f, v120
	v_exp_f32_e32 v126, v126
	v_pk_fma_f32 v[112:113], v[112:113], s[0:1], v[128:129] op_sel_hi:[1,0,1]
	v_pk_fma_f32 v[114:115], v[114:115], s[0:1], v[130:131] op_sel_hi:[1,0,1]
	v_min_f32_e32 v112, 0x40e00000, v112
	v_add_f32_e32 v126, 1.0, v126
	v_rcp_f32_e32 v126, v126
	v_med3_f32 v113, v113, s65, v146
	v_pk_fma_f32 v[108:109], v[108:109], s[0:1], v[132:133] op_sel_hi:[1,0,1]
	v_mul_f32_e32 v120, v120, v126
	v_mul_f32_e32 v120, v121, v120
	v_min_f32_e32 v121, 0x40e00000, v122
	v_med3_f32 v122, v123, s65, v146
	v_mul_f32_e32 v123, 0xc01d265f, v121
	v_exp_f32_e32 v123, v123
	v_min_f32_e32 v108, 0x40e00000, v108
	v_med3_f32 v109, v109, s65, v146
	v_add_f32_e32 v123, 1.0, v123
	v_rcp_f32_e32 v123, v123
	v_pk_fma_f32 v[110:111], v[110:111], s[0:1], v[134:135] op_sel_hi:[1,0,1]
	v_pk_fma_f32 v[104:105], v[104:105], s[0:1], v[128:129] op_sel_hi:[1,0,1]
	v_mul_f32_e32 v121, v121, v123
	v_mul_f32_e32 v122, v122, v121
	v_mov_b32_e32 v121, v137
	v_cvt_pk_fp8_f32 v121, v124, v125
	v_min_f32_e32 v104, 0x40e00000, v104
	v_med3_f32 v105, v105, s65, v146
	v_pk_fma_f32 v[106:107], v[106:107], s[0:1], v[130:131] op_sel_hi:[1,0,1]
	v_cvt_pk_fp8_f32 v121, v120, v122 op_sel:[0,0,1]
	v_mul_f32_e32 v122, 0xc01d265f, v116
	v_exp_f32_e32 v122, v122
	v_pk_fma_f32 v[100:101], v[100:101], s[0:1], v[132:133] op_sel_hi:[1,0,1]
	v_pk_fma_f32 v[102:103], v[102:103], s[0:1], v[134:135] op_sel_hi:[1,0,1]
	v_add_f32_e32 v122, 1.0, v122
	v_rcp_f32_e32 v122, v122
	v_min_f32_e32 v100, 0x40e00000, v100
	v_med3_f32 v101, v101, s65, v146
	v_mul_f32_e32 v116, v116, v122
	v_mul_f32_e32 v116, v117, v116
	v_min_f32_e32 v117, 0x40e00000, v118
	v_med3_f32 v118, v119, s65, v146
	v_mul_f32_e32 v119, 0xc01d265f, v117
	v_exp_f32_e32 v119, v119
	v_pk_fma_f32 v[96:97], v[96:97], s[0:1], v[128:129] op_sel_hi:[1,0,1]
	v_pk_fma_f32 v[98:99], v[98:99], s[0:1], v[130:131] op_sel_hi:[1,0,1]
	v_add_f32_e32 v119, 1.0, v119
	v_rcp_f32_e32 v119, v119
	v_min_f32_e32 v96, 0x40e00000, v96
	v_med3_f32 v97, v97, s65, v146
	v_mul_f32_e32 v117, v117, v119
	v_mul_f32_e32 v117, v118, v117
	v_mul_f32_e32 v118, 0xc01d265f, v112
	v_exp_f32_e32 v118, v118
	v_mul_u32_u24_e32 v120, 0x90, v150
	v_add3_u32 v120, s63, v151, v120
	v_add_f32_e32 v118, 1.0, v118
	v_rcp_f32_e32 v118, v118
	s_nop 0
	v_mul_f32_e32 v112, v112, v118
	v_mul_f32_e32 v113, v113, v112
	v_min_f32_e32 v112, 0x40e00000, v114
	v_med3_f32 v114, v115, s65, v146
	v_mul_f32_e32 v115, 0xc01d265f, v112
	v_exp_f32_e32 v115, v115
	s_nop 0
	v_add_f32_e32 v115, 1.0, v115
	v_rcp_f32_e32 v115, v115
	s_nop 0
	v_mul_f32_e32 v112, v112, v115
	v_mul_f32_e32 v114, v114, v112
	v_mov_b32_e32 v112, v137
	v_cvt_pk_fp8_f32 v112, v116, v117
	s_nop 0
	v_cvt_pk_fp8_f32 v112, v113, v114 op_sel:[0,0,1]
	v_mul_f32_e32 v113, 0xc01d265f, v108
	v_exp_f32_e32 v113, v113
	s_nop 0
	v_add_f32_e32 v113, 1.0, v113
; #define LAS __attribute__((address_space(3)))
; __device__ __forceinline__ unsigned pack4_fp8(float a, float b, float c, float d) { int r = 0; r = __builtin_amdgcn_cvt_pk_fp8_f32(a, b, r, false); r = __builtin_amdgcn_cvt_pk_fp8_f32(c, d, r, true); return (unsigned)r; }
;     __device__ __forceinline__ void operator()(const f32x4 (&acc)[2][2][4][2], const Unit& u, int wr, int wc, int fr, int fq) const {
;     ...
;                 for (int m = 0; m < 4; ++m) {
;                     const f32x4 v0 = acc[ai][bj][m][0] * W8_INV + c0v, v1 = acc[ai][bj][m][1] * W8_INV + c1v;
;                     float o[4];
; #pragma unroll
;                     for (int j = 0; j < 4; ++j) { const float gt = fminf(j < 2 ? v0[2 * j] : v1[2 * j - 4], SW_LIMIT); const float up = fminf(fmaxf(j < 2 ? v0[2 * j + 1] : v1[2 * j - 3], -SW_LIMIT), SW_LIMIT);
;                         o[j] = (up + 1.0f) * (gt * __builtin_amdgcn_rcpf(1.0f + __builtin_amdgcn_exp2f(gt * (-SW_ALPHA * 1.4426950408889634f)))); }
;                     *(LAS unsigned*)(buf + (m * 16 + fr) * 144 + bj * 64 + wc * 16 + fq * 4) = pack4_fp8(o[0], o[1], o[2], o[3]); } }
	v_rcp_f32_e32 v113, v113
	s_nop 0
	v_mul_f32_e32 v108, v108, v113
	v_mul_f32_e32 v108, v109, v108
	v_min_f32_e32 v109, 0x40e00000, v110
	v_med3_f32 v110, v111, s65, v146
	v_mul_f32_e32 v111, 0xc01d265f, v109
	v_exp_f32_e32 v111, v111
	s_nop 0
	v_add_f32_e32 v111, 1.0, v111
	v_rcp_f32_e32 v111, v111
	s_nop 0
	v_mul_f32_e32 v109, v109, v111
	v_mul_f32_e32 v109, v110, v109
	v_mul_f32_e32 v110, 0xc01d265f, v104
	v_exp_f32_e32 v110, v110
	s_nop 0
	v_add_f32_e32 v110, 1.0, v110
	v_rcp_f32_e32 v110, v110
	s_nop 0
	v_mul_f32_e32 v104, v104, v110
	v_mul_f32_e32 v104, v105, v104
	v_min_f32_e32 v105, 0x40e00000, v106
	v_med3_f32 v106, v107, s65, v146
	v_mul_f32_e32 v107, 0xc01d265f, v105
	v_exp_f32_e32 v107, v107
	s_nop 0
	v_add_f32_e32 v107, 1.0, v107
	v_rcp_f32_e32 v107, v107
	s_nop 0
	v_mul_f32_e32 v105, v105, v107
	v_mul_f32_e32 v106, v106, v105
	v_mov_b32_e32 v105, v137
	v_cvt_pk_fp8_f32 v105, v108, v109
	s_nop 0
	v_cvt_pk_fp8_f32 v105, v104, v106 op_sel:[0,0,1]
	v_mul_f32_e32 v104, 0xc01d265f, v100
	v_exp_f32_e32 v104, v104
	s_nop 0
	v_add_f32_e32 v104, 1.0, v104
	v_rcp_f32_e32 v104, v104
	s_nop 0
	v_mul_f32_e32 v100, v100, v104
	v_mul_f32_e32 v100, v101, v100
	v_min_f32_e32 v101, 0x40e00000, v102
	v_med3_f32 v102, v103, s65, v146
	v_mul_f32_e32 v103, 0xc01d265f, v101
	v_exp_f32_e32 v103, v103
	v_mov_b32_e32 v104, v137
	v_add_f32_e32 v103, 1.0, v103
	v_rcp_f32_e32 v103, v103
	s_nop 0
	v_mul_f32_e32 v101, v101, v103
	v_mul_f32_e32 v101, v102, v101
	v_mul_f32_e32 v102, 0xc01d265f, v96
	v_exp_f32_e32 v102, v102
	v_cvt_pk_fp8_f32 v104, v100, v101
	v_add_f32_e32 v102, 1.0, v102
	v_rcp_f32_e32 v102, v102
	s_nop 0
	v_mul_f32_e32 v96, v96, v102
	v_mul_f32_e32 v96, v97, v96
	v_min_f32_e32 v97, 0x40e00000, v98
	v_med3_f32 v98, v99, s65, v146
	v_mul_f32_e32 v99, 0xc01d265f, v97
	v_exp_f32_e32 v99, v99
	s_nop 0
	v_add_f32_e32 v99, 1.0, v99
	v_rcp_f32_e32 v99, v99
	s_nop 0
	v_mul_f32_e32 v97, v97, v99
	v_mul_f32_e32 v97, v98, v97
	v_cvt_pk_fp8_f32 v104, v96, v97 op_sel:[0,0,1]
	global_load_dwordx4 v[96:99], v149, s[10:11] offset:528
	global_load_dwordx4 v[100:103], v149, s[10:11] offset:512
	s_waitcnt vmcnt(0)
	v_add_f32_e32 v97, 1.0, v97
	v_add_f32_e32 v99, 1.0, v99
	v_add_f32_e32 v101, 1.0, v101
	v_add_f32_e32 v103, 1.0, v103
	v_pk_fma_f32 v[88:89], v[88:89], s[0:1], v[96:97] op_sel_hi:[1,0,1]
	s_waitcnt vmcnt(0)
	v_pk_fma_f32 v[92:93], v[92:93], s[0:1], v[100:101] op_sel_hi:[1,0,1]
	v_pk_fma_f32 v[94:95], v[94:95], s[0:1], v[102:103] op_sel_hi:[1,0,1]
	v_min_f32_e32 v92, 0x40e00000, v92
	v_mul_f32_e32 v106, 0xc01d265f, v92
	v_exp_f32_e32 v106, v106
	v_med3_f32 v93, v93, s65, v146
	v_min_f32_e32 v88, 0x40e00000, v88
	v_add_f32_e32 v106, 1.0, v106
	v_rcp_f32_e32 v106, v106
	v_med3_f32 v89, v89, s65, v146
	v_pk_fma_f32 v[90:91], v[90:91], s[0:1], v[98:99] op_sel_hi:[1,0,1]
	v_mul_f32_e32 v92, v92, v106
	v_mul_f32_e32 v92, v93, v92
	v_min_f32_e32 v93, 0x40e00000, v94
	v_med3_f32 v94, v95, s65, v146
	v_mul_f32_e32 v95, 0xc01d265f, v93
	v_exp_f32_e32 v95, v95
	v_pk_fma_f32 v[84:85], v[84:85], s[0:1], v[100:101] op_sel_hi:[1,0,1]
	v_pk_fma_f32 v[86:87], v[86:87], s[0:1], v[102:103] op_sel_hi:[1,0,1]
	v_add_f32_e32 v95, 1.0, v95
	v_rcp_f32_e32 v95, v95
	v_min_f32_e32 v84, 0x40e00000, v84
	v_med3_f32 v85, v85, s65, v146
	v_mul_f32_e32 v93, v93, v95
	v_mul_f32_e32 v93, v94, v93
	v_mul_f32_e32 v94, 0xc01d265f, v88
	v_exp_f32_e32 v94, v94
	v_pk_fma_f32 v[80:81], v[80:81], s[0:1], v[96:97] op_sel_hi:[1,0,1]
	v_pk_fma_f32 v[82:83], v[82:83], s[0:1], v[98:99] op_sel_hi:[1,0,1]
	v_min_f32_e32 v80, 0x40e00000, v80
	v_add_f32_e32 v94, 1.0, v94
	v_rcp_f32_e32 v94, v94
	v_med3_f32 v81, v81, s65, v146
	v_pk_fma_f32 v[76:77], v[76:77], s[0:1], v[100:101] op_sel_hi:[1,0,1]
	v_mul_f32_e32 v88, v88, v94
	v_mul_f32_e32 v88, v89, v88
	v_min_f32_e32 v89, 0x40e00000, v90
	v_med3_f32 v90, v91, s65, v146
	v_mul_f32_e32 v91, 0xc01d265f, v89
	v_exp_f32_e32 v91, v91
	v_min_f32_e32 v76, 0x40e00000, v76
	v_med3_f32 v77, v77, s65, v146
	v_add_f32_e32 v91, 1.0, v91
	v_rcp_f32_e32 v91, v91
	v_pk_fma_f32 v[78:79], v[78:79], s[0:1], v[102:103] op_sel_hi:[1,0,1]
	v_pk_fma_f32 v[72:73], v[72:73], s[0:1], v[96:97] op_sel_hi:[1,0,1]
	v_mul_f32_e32 v89, v89, v91
	v_mul_f32_e32 v89, v90, v89
	v_mov_b32_e32 v90, v137
	v_cvt_pk_fp8_f32 v90, v92, v93
	v_min_f32_e32 v72, 0x40e00000, v72
	v_med3_f32 v73, v73, s65, v146
	v_pk_fma_f32 v[74:75], v[74:75], s[0:1], v[98:99] op_sel_hi:[1,0,1]
	v_cvt_pk_fp8_f32 v90, v88, v89 op_sel:[0,0,1]
	v_mul_f32_e32 v88, 0xc01d265f, v84
	v_exp_f32_e32 v88, v88
	v_pk_fma_f32 v[68:69], v[68:69], s[0:1], v[100:101] op_sel_hi:[1,0,1]
	v_pk_fma_f32 v[70:71], v[70:71], s[0:1], v[102:103] op_sel_hi:[1,0,1]
	v_add_f32_e32 v88, 1.0, v88
	v_rcp_f32_e32 v88, v88
	v_min_f32_e32 v68, 0x40e00000, v68
	v_med3_f32 v69, v69, s65, v146
	v_mul_f32_e32 v84, v84, v88
	v_mul_f32_e32 v84, v85, v84
	v_min_f32_e32 v85, 0x40e00000, v86
	v_med3_f32 v86, v87, s65, v146
	v_mul_f32_e32 v87, 0xc01d265f, v85
	v_exp_f32_e32 v87, v87
	v_pk_fma_f32 v[64:65], v[64:65], s[0:1], v[96:97] op_sel_hi:[1,0,1]
	v_pk_fma_f32 v[66:67], v[66:67], s[0:1], v[98:99] op_sel_hi:[1,0,1]
	v_add_f32_e32 v87, 1.0, v87
	v_rcp_f32_e32 v87, v87
	v_min_f32_e32 v64, 0x40e00000, v64
	v_med3_f32 v65, v65, s65, v146
	v_mul_f32_e32 v85, v85, v87
	v_mul_f32_e32 v85, v86, v85
	v_mul_f32_e32 v86, 0xc01d265f, v80
	v_exp_f32_e32 v86, v86
	ds_write2_b32 v120, v121, v90 offset1:16
	v_add_f32_e32 v86, 1.0, v86
	v_rcp_f32_e32 v86, v86
	s_nop 0
	v_mul_f32_e32 v80, v80, v86
	v_mul_f32_e32 v80, v81, v80
	v_min_f32_e32 v81, 0x40e00000, v82
	v_med3_f32 v82, v83, s65, v146
	v_mul_f32_e32 v83, 0xc01d265f, v81
	v_exp_f32_e32 v83, v83
	s_nop 0
; #define LAS __attribute__((address_space(3)))
; __device__ __forceinline__ unsigned pack4_fp8(float a, float b, float c, float d) { int r = 0; r = __builtin_amdgcn_cvt_pk_fp8_f32(a, b, r, false); r = __builtin_amdgcn_cvt_pk_fp8_f32(c, d, r, true); return (unsigned)r; }
;     __device__ __forceinline__ void operator()(const f32x4 (&acc)[2][2][4][2], const Unit& u, int wr, int wc, int fr, int fq) const {
;     ...
;                 for (int m = 0; m < 4; ++m) {
;                     const f32x4 v0 = acc[ai][bj][m][0] * W8_INV + c0v, v1 = acc[ai][bj][m][1] * W8_INV + c1v;
;                     float o[4];
; #pragma unroll
;                     for (int j = 0; j < 4; ++j) { const float gt = fminf(j < 2 ? v0[2 * j] : v1[2 * j - 4], SW_LIMIT); const float up = fminf(fmaxf(j < 2 ? v0[2 * j + 1] : v1[2 * j - 3], -SW_LIMIT), SW_LIMIT);
;                         o[j] = (up + 1.0f) * (gt * __builtin_amdgcn_rcpf(1.0f + __builtin_amdgcn_exp2f(gt * (-SW_ALPHA * 1.4426950408889634f)))); }
;                     *(LAS unsigned*)(buf + (m * 16 + fr) * 144 + bj * 64 + wc * 16 + fq * 4) = pack4_fp8(o[0], o[1], o[2], o[3]); } }
;             asm volatile("s_waitcnt lgkmcnt(0)" ::: "memory"); __builtin_amdgcn_s_barrier(); asm volatile("" ::: "memory");
;             {   const int l2 = fr + 16 * fq;
; #pragma unroll
;                 for (int i = 0; i < 2; ++i) { const int idx = wc * 64 + l2 + i * 256, row = idx >> 3, ck = idx & 7;
;                     const u32x4 w = *(const LAS u32x4*)(buf + row * 144 + ck * 16);
;                     *(u32x4*)(act + (size_t)(u.pm * 256 + ai * 128 + wr * 64 + row) * DFF + u.pn * 128 + ck * 16) = w; } }
;             asm volatile("s_waitcnt lgkmcnt(0)" ::: "memory"); __builtin_amdgcn_s_barrier(); asm volatile("" ::: "memory");
	v_add_f32_e32 v83, 1.0, v83
	v_rcp_f32_e32 v83, v83
	s_nop 0
	v_mul_f32_e32 v81, v81, v83
	v_mul_f32_e32 v81, v82, v81
	v_mov_b32_e32 v82, v137
	v_cvt_pk_fp8_f32 v82, v84, v85
	s_nop 0
	v_cvt_pk_fp8_f32 v82, v80, v81 op_sel:[0,0,1]
	v_mul_f32_e32 v81, 0xc01d265f, v76
	v_exp_f32_e32 v81, v81
	v_add_u32_e32 v80, 0x800, v120
	ds_write2_b32 v80, v112, v82 offset0:64 offset1:80
	v_add_f32_e32 v81, 1.0, v81
	v_rcp_f32_e32 v81, v81
	s_nop 0
	v_mul_f32_e32 v76, v76, v81
	v_mul_f32_e32 v76, v77, v76
	v_min_f32_e32 v77, 0x40e00000, v78
	v_med3_f32 v78, v79, s65, v146
	v_mul_f32_e32 v79, 0xc01d265f, v77
	v_exp_f32_e32 v79, v79
	s_nop 0
	v_add_f32_e32 v79, 1.0, v79
	v_rcp_f32_e32 v79, v79
	s_nop 0
	v_mul_f32_e32 v77, v77, v79
	v_mul_f32_e32 v77, v78, v77
	v_mul_f32_e32 v78, 0xc01d265f, v72
	v_exp_f32_e32 v78, v78
	s_nop 0
	v_add_f32_e32 v78, 1.0, v78
	v_rcp_f32_e32 v78, v78
	s_nop 0
	v_mul_f32_e32 v72, v72, v78
	v_mul_f32_e32 v72, v73, v72
	v_min_f32_e32 v73, 0x40e00000, v74
	v_med3_f32 v74, v75, s65, v146
	v_mul_f32_e32 v75, 0xc01d265f, v73
	v_exp_f32_e32 v75, v75
	s_nop 0
	v_add_f32_e32 v75, 1.0, v75
	v_rcp_f32_e32 v75, v75
	s_nop 0
	v_mul_f32_e32 v73, v73, v75
	v_mul_f32_e32 v73, v74, v73
	v_mov_b32_e32 v74, v137
	v_cvt_pk_fp8_f32 v74, v76, v77
	s_nop 0
	v_cvt_pk_fp8_f32 v74, v72, v73 op_sel:[0,0,1]
	v_mul_f32_e32 v73, 0xc01d265f, v68
	v_exp_f32_e32 v73, v73
	v_add_u32_e32 v72, 0x1000, v120
	ds_write2_b32 v72, v105, v74 offset0:128 offset1:144
	v_or_b32_e32 v74, 32, v148
	v_add_f32_e32 v73, 1.0, v73
	v_rcp_f32_e32 v73, v73
	s_nop 0
	v_mul_f32_e32 v68, v68, v73
	v_mul_f32_e32 v68, v69, v68
	v_min_f32_e32 v69, 0x40e00000, v70
	v_med3_f32 v70, v71, s65, v146
	v_mul_f32_e32 v71, 0xc01d265f, v69
	v_exp_f32_e32 v71, v71
	v_add_u32_e32 v73, 0x1800, v120
	v_add_f32_e32 v71, 1.0, v71
	v_rcp_f32_e32 v71, v71
	s_nop 0
	v_mul_f32_e32 v69, v69, v71
	v_mul_f32_e32 v69, v70, v69
	v_mul_f32_e32 v70, 0xc01d265f, v64
	v_exp_f32_e32 v70, v70
	s_nop 0
	v_add_f32_e32 v70, 1.0, v70
	v_rcp_f32_e32 v70, v70
	s_nop 0
	v_mul_f32_e32 v64, v64, v70
	v_mul_f32_e32 v64, v65, v64
	v_min_f32_e32 v65, 0x40e00000, v66
	v_med3_f32 v66, v67, s65, v146
	v_mul_f32_e32 v67, 0xc01d265f, v65
	v_exp_f32_e32 v67, v67
	s_nop 0
	v_add_f32_e32 v67, 1.0, v67
	v_rcp_f32_e32 v67, v67
	s_nop 0
	v_mul_f32_e32 v65, v65, v67
	v_mul_f32_e32 v65, v66, v65
	v_mov_b32_e32 v66, v137
	v_cvt_pk_fp8_f32 v66, v68, v69
	v_or_b32_e32 v68, s8, v148
	v_ashrrev_i32_e32 v69, 31, v68
	v_lshlrev_b64 v[68:69], 11, v[68:69]
	v_cvt_pk_fp8_f32 v66, v64, v65 op_sel:[0,0,1]
	v_lshl_add_u64 v[68:69], s[4:5], 0, v[68:69]
	v_lshl_add_u64 v[68:69], v[68:69], 0, s[38:39]
	v_lshl_add_u64 v[68:69], v[68:69], 0, v[136:137]
	ds_write2_b32 v73, v104, v66 offset0:192 offset1:208
	s_waitcnt lgkmcnt(0)
	s_barrier
	ds_read_b128 v[64:67], v147
	s_waitcnt lgkmcnt(0)
	global_store_dwordx4 v[68:69], v[64:67], off
	v_or_b32_e32 v68, s8, v74
	ds_read_b128 v[64:67], v147 offset:4608
	v_ashrrev_i32_e32 v69, 31, v68
	v_lshlrev_b64 v[68:69], 11, v[68:69]
	v_lshl_add_u64 v[68:69], s[4:5], 0, v[68:69]
	v_lshl_add_u64 v[68:69], v[68:69], 0, s[38:39]
	v_lshl_add_u64 v[68:69], v[68:69], 0, v[136:137]
	s_waitcnt lgkmcnt(0)
	global_store_dwordx4 v[68:69], v[64:67], off
	s_waitcnt lgkmcnt(0)
	s_barrier
	global_load_dwordx4 v[64:67], v149, s[10:11] offset:16
	global_load_dwordx4 v[68:71], v149, s[10:11]
	s_addk_i32 s8, 0x80
	s_waitcnt vmcnt(0)
	v_add_f32_e32 v65, 1.0, v65
	v_add_f32_e32 v67, 1.0, v67
	v_add_f32_e32 v69, 1.0, v69
	v_add_f32_e32 v71, 1.0, v71
	v_pk_fma_f32 v[56:57], v[56:57], s[0:1], v[64:65] op_sel_hi:[1,0,1]
	s_waitcnt vmcnt(0)
	v_pk_fma_f32 v[60:61], v[60:61], s[0:1], v[68:69] op_sel_hi:[1,0,1]
	v_pk_fma_f32 v[62:63], v[62:63], s[0:1], v[70:71] op_sel_hi:[1,0,1]
	v_min_f32_e32 v60, 0x40e00000, v60
	v_mul_f32_e32 v75, 0xc01d265f, v60
	v_exp_f32_e32 v75, v75
	v_med3_f32 v61, v61, s65, v146
	v_min_f32_e32 v56, 0x40e00000, v56
	v_add_f32_e32 v75, 1.0, v75
	v_rcp_f32_e32 v75, v75
	v_med3_f32 v57, v57, s65, v146
	v_pk_fma_f32 v[58:59], v[58:59], s[0:1], v[66:67] op_sel_hi:[1,0,1]
	v_mul_f32_e32 v60, v60, v75
	v_mul_f32_e32 v60, v61, v60
	v_min_f32_e32 v61, 0x40e00000, v62
	v_med3_f32 v62, v63, s65, v146
	v_mul_f32_e32 v63, 0xc01d265f, v61
	v_exp_f32_e32 v63, v63
	v_pk_fma_f32 v[52:53], v[52:53], s[0:1], v[68:69] op_sel_hi:[1,0,1]
	v_pk_fma_f32 v[54:55], v[54:55], s[0:1], v[70:71] op_sel_hi:[1,0,1]
	v_add_f32_e32 v63, 1.0, v63
	v_rcp_f32_e32 v63, v63
	v_min_f32_e32 v52, 0x40e00000, v52
	v_med3_f32 v53, v53, s65, v146
	v_mul_f32_e32 v61, v61, v63
	v_mul_f32_e32 v61, v62, v61
	v_mul_f32_e32 v62, 0xc01d265f, v56
	v_exp_f32_e32 v62, v62
	v_pk_fma_f32 v[48:49], v[48:49], s[0:1], v[64:65] op_sel_hi:[1,0,1]
	v_pk_fma_f32 v[50:51], v[50:51], s[0:1], v[66:67] op_sel_hi:[1,0,1]
	v_min_f32_e32 v48, 0x40e00000, v48
	v_add_f32_e32 v62, 1.0, v62
	v_rcp_f32_e32 v62, v62
	v_med3_f32 v49, v49, s65, v146
	v_pk_fma_f32 v[44:45], v[44:45], s[0:1], v[68:69] op_sel_hi:[1,0,1]
	v_mul_f32_e32 v56, v56, v62
	v_mul_f32_e32 v57, v57, v56
	v_min_f32_e32 v56, 0x40e00000, v58
	v_med3_f32 v58, v59, s65, v146
	v_mul_f32_e32 v59, 0xc01d265f, v56
	v_exp_f32_e32 v59, v59
	v_min_f32_e32 v44, 0x40e00000, v44
	v_med3_f32 v45, v45, s65, v146
	v_add_f32_e32 v59, 1.0, v59
	v_rcp_f32_e32 v59, v59
	v_pk_fma_f32 v[46:47], v[46:47], s[0:1], v[70:71] op_sel_hi:[1,0,1]
	v_pk_fma_f32 v[40:41], v[40:41], s[0:1], v[64:65] op_sel_hi:[1,0,1]
	v_mul_f32_e32 v56, v56, v59
	v_mul_f32_e32 v58, v58, v56
	v_mov_b32_e32 v56, v137
	v_cvt_pk_fp8_f32 v56, v60, v61
	v_min_f32_e32 v40, 0x40e00000, v40
	v_med3_f32 v41, v41, s65, v146
	v_pk_fma_f32 v[42:43], v[42:43], s[0:1], v[66:67] op_sel_hi:[1,0,1]
; #define LAS __attribute__((address_space(3)))
; __device__ __forceinline__ unsigned pack4_fp8(float a, float b, float c, float d) { int r = 0; r = __builtin_amdgcn_cvt_pk_fp8_f32(a, b, r, false); r = __builtin_amdgcn_cvt_pk_fp8_f32(c, d, r, true); return (unsigned)r; }
;     __device__ __forceinline__ void operator()(const f32x4 (&acc)[2][2][4][2], const Unit& u, int wr, int wc, int fr, int fq) const {
;     ...
;                 for (int m = 0; m < 4; ++m) {
;                     const f32x4 v0 = acc[ai][bj][m][0] * W8_INV + c0v, v1 = acc[ai][bj][m][1] * W8_INV + c1v;
;                     float o[4];
; #pragma unroll
;                     for (int j = 0; j < 4; ++j) { const float gt = fminf(j < 2 ? v0[2 * j] : v1[2 * j - 4], SW_LIMIT); const float up = fminf(fmaxf(j < 2 ? v0[2 * j + 1] : v1[2 * j - 3], -SW_LIMIT), SW_LIMIT);
;                         o[j] = (up + 1.0f) * (gt * __builtin_amdgcn_rcpf(1.0f + __builtin_amdgcn_exp2f(gt * (-SW_ALPHA * 1.4426950408889634f)))); }
;                     *(LAS unsigned*)(buf + (m * 16 + fr) * 144 + bj * 64 + wc * 16 + fq * 4) = pack4_fp8(o[0], o[1], o[2], o[3]); } }
	v_cvt_pk_fp8_f32 v56, v57, v58 op_sel:[0,0,1]
	v_mul_f32_e32 v57, 0xc01d265f, v52
	v_exp_f32_e32 v57, v57
	v_pk_fma_f32 v[36:37], v[36:37], s[0:1], v[68:69] op_sel_hi:[1,0,1]
	v_pk_fma_f32 v[38:39], v[38:39], s[0:1], v[70:71] op_sel_hi:[1,0,1]
	v_add_f32_e32 v57, 1.0, v57
	v_rcp_f32_e32 v57, v57
	v_min_f32_e32 v36, 0x40e00000, v36
	v_med3_f32 v37, v37, s65, v146
	v_mul_f32_e32 v52, v52, v57
	v_mul_f32_e32 v52, v53, v52
	v_min_f32_e32 v53, 0x40e00000, v54
	v_med3_f32 v54, v55, s65, v146
	v_mul_f32_e32 v55, 0xc01d265f, v53
	v_exp_f32_e32 v55, v55
	v_pk_fma_f32 v[32:33], v[32:33], s[0:1], v[64:65] op_sel_hi:[1,0,1]
	v_pk_fma_f32 v[34:35], v[34:35], s[0:1], v[66:67] op_sel_hi:[1,0,1]
	v_add_f32_e32 v55, 1.0, v55
	v_rcp_f32_e32 v55, v55
	v_min_f32_e32 v32, 0x40e00000, v32
	v_med3_f32 v33, v33, s65, v146
	v_mul_f32_e32 v53, v53, v55
	v_mul_f32_e32 v53, v54, v53
	v_mul_f32_e32 v54, 0xc01d265f, v48
	v_exp_f32_e32 v54, v54
	s_nop 0
	v_add_f32_e32 v54, 1.0, v54
	v_rcp_f32_e32 v54, v54
	s_nop 0
	v_mul_f32_e32 v48, v48, v54
	v_mul_f32_e32 v49, v49, v48
	v_min_f32_e32 v48, 0x40e00000, v50
	v_med3_f32 v50, v51, s65, v146
	v_mul_f32_e32 v51, 0xc01d265f, v48
	v_exp_f32_e32 v51, v51
	s_nop 0
	v_add_f32_e32 v51, 1.0, v51
	v_rcp_f32_e32 v51, v51
	s_nop 0
	v_mul_f32_e32 v48, v48, v51
	v_mul_f32_e32 v50, v50, v48
	v_mov_b32_e32 v48, v137
	v_cvt_pk_fp8_f32 v48, v52, v53
	s_nop 0
	v_cvt_pk_fp8_f32 v48, v49, v50 op_sel:[0,0,1]
	v_mul_f32_e32 v49, 0xc01d265f, v44
	v_exp_f32_e32 v49, v49
	s_nop 0
	v_add_f32_e32 v49, 1.0, v49
	v_rcp_f32_e32 v49, v49
	s_nop 0
	v_mul_f32_e32 v44, v44, v49
	v_mul_f32_e32 v44, v45, v44
	v_min_f32_e32 v45, 0x40e00000, v46
	v_med3_f32 v46, v47, s65, v146
	v_mul_f32_e32 v47, 0xc01d265f, v45
	v_exp_f32_e32 v47, v47
	s_nop 0
	v_add_f32_e32 v47, 1.0, v47
	v_rcp_f32_e32 v47, v47
	s_nop 0
	v_mul_f32_e32 v45, v45, v47
	v_mul_f32_e32 v45, v46, v45
	v_mul_f32_e32 v46, 0xc01d265f, v40
	v_exp_f32_e32 v46, v46
	s_nop 0
	v_add_f32_e32 v46, 1.0, v46
	v_rcp_f32_e32 v46, v46
	s_nop 0
	v_mul_f32_e32 v40, v40, v46
	v_mul_f32_e32 v40, v41, v40
	v_min_f32_e32 v41, 0x40e00000, v42
	v_med3_f32 v42, v43, s65, v146
	v_mul_f32_e32 v43, 0xc01d265f, v41
	v_exp_f32_e32 v43, v43
	s_nop 0
	v_add_f32_e32 v43, 1.0, v43
	v_rcp_f32_e32 v43, v43
	s_nop 0
	v_mul_f32_e32 v41, v41, v43
	v_mul_f32_e32 v42, v42, v41
	v_mov_b32_e32 v41, v137
	v_cvt_pk_fp8_f32 v41, v44, v45
	s_nop 0
	v_cvt_pk_fp8_f32 v41, v40, v42 op_sel:[0,0,1]
	v_mul_f32_e32 v40, 0xc01d265f, v36
	v_exp_f32_e32 v40, v40
	s_nop 0
	v_add_f32_e32 v40, 1.0, v40
	v_rcp_f32_e32 v40, v40
	s_nop 0
	v_mul_f32_e32 v36, v36, v40
	v_mul_f32_e32 v36, v37, v36
	v_min_f32_e32 v37, 0x40e00000, v38
	v_med3_f32 v38, v39, s65, v146
	v_mul_f32_e32 v39, 0xc01d265f, v37
	v_exp_f32_e32 v39, v39
	v_mov_b32_e32 v40, v137
	v_add_f32_e32 v39, 1.0, v39
	v_rcp_f32_e32 v39, v39
	s_nop 0
	v_mul_f32_e32 v37, v37, v39
	v_mul_f32_e32 v37, v38, v37
	v_mul_f32_e32 v38, 0xc01d265f, v32
	v_exp_f32_e32 v38, v38
	v_cvt_pk_fp8_f32 v40, v36, v37
	v_add_f32_e32 v38, 1.0, v38
	v_rcp_f32_e32 v38, v38
	s_nop 0
	v_mul_f32_e32 v32, v32, v38
	v_mul_f32_e32 v32, v33, v32
	v_min_f32_e32 v33, 0x40e00000, v34
	v_med3_f32 v34, v35, s65, v146
	v_mul_f32_e32 v35, 0xc01d265f, v33
	v_exp_f32_e32 v35, v35
	s_nop 0
	v_add_f32_e32 v35, 1.0, v35
	v_rcp_f32_e32 v35, v35
	s_nop 0
	v_mul_f32_e32 v33, v33, v35
	v_mul_f32_e32 v33, v34, v33
	v_cvt_pk_fp8_f32 v40, v32, v33 op_sel:[0,0,1]
	global_load_dwordx4 v[32:35], v149, s[10:11] offset:528
	global_load_dwordx4 v[36:39], v149, s[10:11] offset:512
	s_waitcnt vmcnt(0)
	v_add_f32_e32 v33, 1.0, v33
	v_add_f32_e32 v35, 1.0, v35
	v_add_f32_e32 v37, 1.0, v37
	v_add_f32_e32 v39, 1.0, v39
	v_pk_fma_f32 v[24:25], v[24:25], s[0:1], v[32:33] op_sel_hi:[1,0,1]
	s_waitcnt vmcnt(0)
; #define LAS __attribute__((address_space(3)))
; __device__ __forceinline__ unsigned pack4_fp8(float a, float b, float c, float d) { int r = 0; r = __builtin_amdgcn_cvt_pk_fp8_f32(a, b, r, false); r = __builtin_amdgcn_cvt_pk_fp8_f32(c, d, r, true); return (unsigned)r; }
; template <class Epi, class Sched, bool FP8 = false>
; __device__ __forceinline__ void gemm_phase(LAS unsigned char* lds, const Gemm g, const Sched& S, const Epi& E, const int wave) {
;     ...
;         if (!has_next) break;
; #pragma unroll
;         for (int a = 0; a < 2; ++a)
; #pragma unroll
;             for (int b = 0; b < 2; ++b)
; #pragma unroll
;                 for (int m = 0; m < 4; ++m)
; #pragma unroll
;                     for (int n = 0; n < 2; ++n) acc[a][b][m][n] = (f32x4){0.f, 0.f, 0.f, 0.f};
;         cur = nxt; cA = nA; cB = nB; ++ui;
;     }
;     PG8_WAIT_V(0);
;     if (wr == 0) PG8_BAR;
;     PG8_BAR;
;     __device__ __forceinline__ void operator()(const f32x4 (&acc)[2][2][4][2], const Unit& u, int wr, int wc, int fr, int fq) const {
;     ...
;                 for (int m = 0; m < 4; ++m) {
;                     const f32x4 v0 = acc[ai][bj][m][0] * W8_INV + c0v, v1 = acc[ai][bj][m][1] * W8_INV + c1v;
;                     float o[4];
; #pragma unroll
;                     for (int j = 0; j < 4; ++j) { const float gt = fminf(j < 2 ? v0[2 * j] : v1[2 * j - 4], SW_LIMIT); const float up = fminf(fmaxf(j < 2 ? v0[2 * j + 1] : v1[2 * j - 3], -SW_LIMIT), SW_LIMIT);
;                         o[j] = (up + 1.0f) * (gt * __builtin_amdgcn_rcpf(1.0f + __builtin_amdgcn_exp2f(gt * (-SW_ALPHA * 1.4426950408889634f)))); }
;                     *(LAS unsigned*)(buf + (m * 16 + fr) * 144 + bj * 64 + wc * 16 + fq * 4) = pack4_fp8(o[0], o[1], o[2], o[3]); } }
;             asm volatile("s_waitcnt lgkmcnt(0)" ::: "memory"); __builtin_amdgcn_s_barrier(); asm volatile("" ::: "memory");
;             {   const int l2 = fr + 16 * fq;
; #pragma unroll
;                 for (int i = 0; i < 2; ++i) { const int idx = wc * 64 + l2 + i * 256, row = idx >> 3, ck = idx & 7;
;                     const u32x4 w = *(const LAS u32x4*)(buf + row * 144 + ck * 16);
;                     *(u32x4*)(act + (size_t)(u.pm * 256 + ai * 128 + wr * 64 + row) * DFF + u.pn * 128 + ck * 16) = w; } }
;             asm volatile("s_waitcnt lgkmcnt(0)" ::: "memory"); __builtin_amdgcn_s_barrier(); asm volatile("" ::: "memory");
	v_pk_fma_f32 v[28:29], v[28:29], s[0:1], v[36:37] op_sel_hi:[1,0,1]
	v_pk_fma_f32 v[30:31], v[30:31], s[0:1], v[38:39] op_sel_hi:[1,0,1]
	v_min_f32_e32 v28, 0x40e00000, v28
	v_mul_f32_e32 v42, 0xc01d265f, v28
	v_exp_f32_e32 v42, v42
	v_med3_f32 v29, v29, s65, v146
	v_min_f32_e32 v24, 0x40e00000, v24
	v_add_f32_e32 v42, 1.0, v42
	v_rcp_f32_e32 v42, v42
	v_med3_f32 v25, v25, s65, v146
	v_pk_fma_f32 v[26:27], v[26:27], s[0:1], v[34:35] op_sel_hi:[1,0,1]
	v_mul_f32_e32 v28, v28, v42
	v_mul_f32_e32 v28, v29, v28
	v_min_f32_e32 v29, 0x40e00000, v30
	v_med3_f32 v30, v31, s65, v146
	v_mul_f32_e32 v31, 0xc01d265f, v29
	v_exp_f32_e32 v31, v31
	v_pk_fma_f32 v[20:21], v[20:21], s[0:1], v[36:37] op_sel_hi:[1,0,1]
	v_pk_fma_f32 v[22:23], v[22:23], s[0:1], v[38:39] op_sel_hi:[1,0,1]
	v_add_f32_e32 v31, 1.0, v31
	v_rcp_f32_e32 v31, v31
	v_min_f32_e32 v20, 0x40e00000, v20
	v_med3_f32 v21, v21, s65, v146
	v_mul_f32_e32 v29, v29, v31
	v_mul_f32_e32 v29, v30, v29
	v_mul_f32_e32 v30, 0xc01d265f, v24
	v_exp_f32_e32 v30, v30
	v_pk_fma_f32 v[16:17], v[16:17], s[0:1], v[32:33] op_sel_hi:[1,0,1]
	v_pk_fma_f32 v[18:19], v[18:19], s[0:1], v[34:35] op_sel_hi:[1,0,1]
	v_min_f32_e32 v16, 0x40e00000, v16
	v_add_f32_e32 v30, 1.0, v30
	v_rcp_f32_e32 v30, v30
	v_med3_f32 v17, v17, s65, v146
	v_pk_fma_f32 v[12:13], v[12:13], s[0:1], v[36:37] op_sel_hi:[1,0,1]
	v_mul_f32_e32 v24, v24, v30
	v_mul_f32_e32 v24, v25, v24
	v_min_f32_e32 v25, 0x40e00000, v26
	v_med3_f32 v26, v27, s65, v146
	v_mul_f32_e32 v27, 0xc01d265f, v25
	v_exp_f32_e32 v27, v27
	v_min_f32_e32 v12, 0x40e00000, v12
	v_med3_f32 v13, v13, s65, v146
	v_add_f32_e32 v27, 1.0, v27
	v_rcp_f32_e32 v27, v27
	v_pk_fma_f32 v[14:15], v[14:15], s[0:1], v[38:39] op_sel_hi:[1,0,1]
	v_pk_fma_f32 v[8:9], v[8:9], s[0:1], v[32:33] op_sel_hi:[1,0,1]
	v_mul_f32_e32 v25, v25, v27
	v_mul_f32_e32 v25, v26, v25
	v_mov_b32_e32 v26, v137
	v_cvt_pk_fp8_f32 v26, v28, v29
	v_min_f32_e32 v8, 0x40e00000, v8
	v_med3_f32 v9, v9, s65, v146
	v_pk_fma_f32 v[10:11], v[10:11], s[0:1], v[34:35] op_sel_hi:[1,0,1]
	v_cvt_pk_fp8_f32 v26, v24, v25 op_sel:[0,0,1]
	v_mul_f32_e32 v24, 0xc01d265f, v20
	v_exp_f32_e32 v24, v24
	v_pk_fma_f32 v[4:5], v[4:5], s[0:1], v[32:33] op_sel_hi:[1,0,1]
	v_pk_fma_f32 v[2:3], v[2:3], s[0:1], v[38:39] op_sel_hi:[1,0,1]
	v_add_f32_e32 v24, 1.0, v24
	v_rcp_f32_e32 v24, v24
	v_min_f32_e32 v4, 0x40e00000, v4
	v_med3_f32 v5, v5, s65, v146
	v_mul_f32_e32 v20, v20, v24
	v_mul_f32_e32 v20, v21, v20
	v_min_f32_e32 v21, 0x40e00000, v22
	v_med3_f32 v22, v23, s65, v146
	v_mul_f32_e32 v23, 0xc01d265f, v21
	v_exp_f32_e32 v23, v23
	v_min_f32_e32 v2, 0x40e00000, v2
	v_pk_fma_f32 v[0:1], v[0:1], s[0:1], v[36:37] op_sel_hi:[1,0,1]
	v_add_f32_e32 v23, 1.0, v23
	v_rcp_f32_e32 v23, v23
	v_med3_f32 v3, v3, s65, v146
	v_min_f32_e32 v0, 0x40e00000, v0
	v_mul_f32_e32 v21, v21, v23
	v_mul_f32_e32 v21, v22, v21
	v_mul_f32_e32 v22, 0xc01d265f, v16
	v_exp_f32_e32 v22, v22
	v_pk_fma_f32 v[6:7], v[6:7], s[0:1], v[34:35] op_sel_hi:[1,0,1]
	v_med3_f32 v1, v1, s65, v146
	v_min_f32_e32 v6, 0x40e00000, v6
	v_add_f32_e32 v22, 1.0, v22
	v_rcp_f32_e32 v22, v22
	ds_write2_b32 v120, v56, v26 offset1:16
	v_mul_f32_e32 v16, v16, v22
	v_mul_f32_e32 v16, v17, v16
	v_min_f32_e32 v17, 0x40e00000, v18
	v_med3_f32 v18, v19, s65, v146
	v_mul_f32_e32 v19, 0xc01d265f, v17
	v_exp_f32_e32 v19, v19
	s_nop 0
	v_add_f32_e32 v19, 1.0, v19
	v_rcp_f32_e32 v19, v19
	s_nop 0
	v_mul_f32_e32 v17, v17, v19
	v_mul_f32_e32 v17, v18, v17
	v_mov_b32_e32 v18, v137
	v_cvt_pk_fp8_f32 v18, v20, v21
	s_nop 0
	v_cvt_pk_fp8_f32 v18, v16, v17 op_sel:[0,0,1]
	v_mul_f32_e32 v16, 0xc01d265f, v12
	v_exp_f32_e32 v16, v16
	ds_write2_b32 v80, v48, v18 offset0:64 offset1:80
	v_add_f32_e32 v16, 1.0, v16
	v_rcp_f32_e32 v16, v16
	s_nop 0
	v_mul_f32_e32 v12, v12, v16
	v_mul_f32_e32 v12, v13, v12
	v_min_f32_e32 v13, 0x40e00000, v14
	v_med3_f32 v14, v15, s65, v146
	v_mul_f32_e32 v15, 0xc01d265f, v13
	v_exp_f32_e32 v15, v15
	s_nop 0
	v_add_f32_e32 v15, 1.0, v15
	v_rcp_f32_e32 v15, v15
	s_nop 0
	v_mul_f32_e32 v13, v13, v15
	v_mul_f32_e32 v13, v14, v13
	v_mul_f32_e32 v14, 0xc01d265f, v8
	v_exp_f32_e32 v14, v14
	s_nop 0
	v_add_f32_e32 v14, 1.0, v14
	v_rcp_f32_e32 v14, v14
	s_nop 0
	v_mul_f32_e32 v8, v8, v14
	v_mul_f32_e32 v8, v9, v8
	v_min_f32_e32 v9, 0x40e00000, v10
	v_med3_f32 v10, v11, s65, v146
	v_mul_f32_e32 v11, 0xc01d265f, v9
	v_exp_f32_e32 v11, v11
	s_nop 0
	v_add_f32_e32 v11, 1.0, v11
	v_rcp_f32_e32 v11, v11
	s_nop 0
	v_mul_f32_e32 v9, v9, v11
	v_mul_f32_e32 v9, v10, v9
	v_mov_b32_e32 v10, v137
	v_cvt_pk_fp8_f32 v10, v12, v13
	s_nop 0
	v_cvt_pk_fp8_f32 v10, v8, v9 op_sel:[0,0,1]
	v_mul_f32_e32 v8, 0xc01d265f, v4
	v_exp_f32_e32 v8, v8
	ds_write2_b32 v72, v41, v10 offset0:128 offset1:144
	v_add_f32_e32 v8, 1.0, v8
	v_rcp_f32_e32 v8, v8
	s_nop 0
	v_mul_f32_e32 v4, v4, v8
	v_mul_f32_e32 v4, v5, v4
	v_mul_f32_e32 v5, 0xc01d265f, v2
	v_exp_f32_e32 v5, v5
	s_nop 0
	v_add_f32_e32 v5, 1.0, v5
	v_rcp_f32_e32 v5, v5
	s_nop 0
	v_mul_f32_e32 v2, v2, v5
	v_mul_f32_e32 v2, v3, v2
	v_mul_f32_e32 v3, 0xc01d265f, v0
	v_exp_f32_e32 v3, v3
	s_nop 0
	v_add_f32_e32 v3, 1.0, v3
	v_rcp_f32_e32 v3, v3
	s_nop 0
	v_mul_f32_e32 v0, v0, v3
	v_mul_f32_e32 v3, 0xc01d265f, v6
	v_exp_f32_e32 v3, v3
	v_mul_f32_e32 v0, v1, v0
	v_med3_f32 v1, v7, s65, v146
	v_add_f32_e32 v3, 1.0, v3
	v_rcp_f32_e32 v3, v3
	s_nop 0
	v_mul_f32_e32 v3, v6, v3
	v_mul_f32_e32 v1, v1, v3
	v_mov_b32_e32 v3, v137
	v_cvt_pk_fp8_f32 v3, v0, v2
	s_nop 0
	v_cvt_pk_fp8_f32 v3, v4, v1 op_sel:[0,0,1]
	v_or_b32_e32 v4, s8, v148
	v_ashrrev_i32_e32 v5, 31, v4
	v_lshlrev_b64 v[4:5], 11, v[4:5]
	ds_write2_b32 v73, v40, v3 offset0:192 offset1:208
	s_waitcnt lgkmcnt(0)
	s_barrier
	ds_read_b128 v[0:3], v147
	v_lshl_add_u64 v[4:5], s[4:5], 0, v[4:5]
	v_lshl_add_u64 v[4:5], v[4:5], 0, s[38:39]
	v_lshl_add_u64 v[4:5], v[4:5], 0, v[136:137]
	s_waitcnt lgkmcnt(0)
	global_store_dwordx4 v[4:5], v[0:3], off
	v_or_b32_e32 v4, s8, v74
	ds_read_b128 v[0:3], v147 offset:4608
	v_ashrrev_i32_e32 v5, 31, v4
	v_lshlrev_b64 v[4:5], 11, v[4:5]
	v_lshl_add_u64 v[4:5], s[4:5], 0, v[4:5]
	v_lshl_add_u64 v[4:5], v[4:5], 0, s[38:39]
	v_lshl_add_u64 v[4:5], v[4:5], 0, v[136:137]
	s_waitcnt lgkmcnt(0)
	global_store_dwordx4 v[4:5], v[0:3], off
	s_waitcnt lgkmcnt(0)
	s_barrier
	s_mov_b32 s38, s67
	s_cbranch_vccz .LBB0_1262
	s_waitcnt vmcnt(0)
	s_cmpk_gt_u32 s1, 0xff
	s_cbranch_scc1 .LBB0_1269
	s_barrier
